# ho2: grid barrier: XCD leader bumps the generation word before its own acquire invalidate; non-leaders issue the invalidate before spinning
# speedup vs baseline: 1.0088x; 1.0066x over previous
; __device__ __forceinline__ unsigned xb_ld(unsigned* p)              { return __hip_atomic_load(p, __ATOMIC_RELAXED, __HIP_MEMORY_SCOPE_AGENT); }
; __device__ __forceinline__ unsigned xb_add(unsigned* p, unsigned v) { return __hip_atomic_fetch_add(p, v, __ATOMIC_RELAXED, __HIP_MEMORY_SCOPE_AGENT); }
; #define XB_SPIN(cond, bar) do { unsigned _sp = 0; while (cond) { __builtin_amdgcn_s_sleep(1); \
;     if ((++_sp & 255u) == 0u) { if (xb_ld(&(bar)[XB_TMO])) break; if (_sp > XB_SPIN_CAP) { atomicAdd(&(bar)[XB_TMO], 1u); break; } } } } while (0)
; __device__ __forceinline__ void xcd_barrier(const XcdBarrier& b) {
;     ...
;         unsigned nloc = b.st[0], nx = b.st[1];
;         if (nloc == 0u) { xcd_barrier_complete(bar, bx_, nloc, nx); b.st[0] = nloc; b.st[1] = nx; }
;         const unsigned old = xb_add(&bar[XB_XSUB(bx_)], 1u);
;         const unsigned gen = old / nloc;
;         if (old + 1u == (gen + 1u) * nloc) {
;             __builtin_amdgcn_fence(__ATOMIC_RELEASE, "agent");
;             asm volatile("s_waitcnt vmcnt(0)" ::: "memory");
;             const unsigned og = xb_add(&bar[XB_TOP], 1u);
;             const unsigned tg = og / nx;
;             if (og + 1u == (tg + 1u) * nx) xb_add(&bar[XB_TOPGEN], 1u);
;             else XB_SPIN(xb_ld(&bar[XB_TOPGEN]) == tg, bar);
;             __builtin_amdgcn_fence(__ATOMIC_ACQUIRE, "agent");
;             xb_add(&bar[XB_XGEN(bx_)], 1u);
;             asm volatile("s_waitcnt vmcnt(0)" ::: "memory");
;         } else {
;             XB_SPIN(xb_ld(&bar[XB_XGEN(bx_)]) == gen, bar);
;             __builtin_amdgcn_fence(__ATOMIC_ACQUIRE, "agent");
;             asm volatile("s_waitcnt vmcnt(0)" ::: "memory");
;         }
.LBB0_528:
	s_lshl_b32 s8, s8, 6
	s_add_i32 s6, s8, 0x500
	s_mov_b32 s7, 0
	s_lshl_b64 s[4:5], s[6:7], 2
	s_add_u32 s4, s38, s4
	s_addc_u32 s5, s39, s5
	v_mov_b32_e32 v1, 1
	v_mov_b64_e32 v[4:5], s[4:5]
	flat_atomic_add v1, v[4:5], v1 sc0
	v_cvt_f32_u32_e32 v3, v2
	v_sub_u32_e32 v4, 0, v2
	v_rcp_iflag_f32_e32 v3, v3
	s_nop 0
	v_mul_f32_e32 v3, 0x4f7ffffe, v3
	v_cvt_u32_f32_e32 v3, v3
	v_mul_lo_u32 v4, v4, v3
	v_mul_hi_u32 v4, v3, v4
	v_add_u32_e32 v3, v3, v4
	s_waitcnt vmcnt(0) lgkmcnt(0)
	v_mul_hi_u32 v3, v1, v3
	v_mul_lo_u32 v5, v3, v2
	v_add_u32_e32 v4, 1, v1
	v_sub_u32_e32 v1, v1, v5
	v_add_u32_e32 v6, 1, v3
	v_cmp_ge_u32_e32 vcc, v1, v2
	v_sub_u32_e32 v5, v1, v2
	s_nop 0
	v_cndmask_b32_e32 v3, v3, v6, vcc
	v_cndmask_b32_e32 v1, v1, v5, vcc
	v_add_u32_e32 v5, 1, v3
	v_cmp_ge_u32_e32 vcc, v1, v2
	s_nop 1
	v_cndmask_b32_e32 v1, v3, v5, vcc
	v_mad_u64_u32 v[2:3], s[4:5], v2, v1, v[2:3]
	v_cmp_ne_u32_e32 vcc, v4, v2
	s_and_saveexec_b64 s[4:5], vcc
	s_xor_b64 s[4:5], exec, s[4:5]
	s_cbranch_execz .LBB0_541
	s_add_i32 s6, s8, 0x900
	s_lshl_b64 s[6:7], s[6:7], 2
	s_add_u32 s10, s38, s6
	s_addc_u32 s11, s39, s7
	v_mov_b64_e32 v[2:3], s[10:11]
	buffer_inv sc1
	flat_load_dword v0, v[2:3] sc1
	s_waitcnt vmcnt(0) lgkmcnt(0)
	v_cmp_eq_u32_e32 vcc, v0, v1
	s_and_saveexec_b64 s[6:7], vcc
	s_cbranch_execz .LBB0_540
	s_mov_b32 s9, 1
	s_mov_b64 s[12:13], 0
	s_branch .LBB0_532

; __device__ __forceinline__ unsigned xb_ld(unsigned* p)              { return __hip_atomic_load(p, __ATOMIC_RELAXED, __HIP_MEMORY_SCOPE_AGENT); }
; #define XB_SPIN(cond, bar) do { unsigned _sp = 0; while (cond) { __builtin_amdgcn_s_sleep(1); \
;     if ((++_sp & 255u) == 0u) { if (xb_ld(&(bar)[XB_TMO])) break; if (_sp > XB_SPIN_CAP) { atomicAdd(&(bar)[XB_TMO], 1u); break; } } } } while (0)
; __device__ __forceinline__ void xcd_barrier(const XcdBarrier& b) {
;     ...
;             XB_SPIN(xb_ld(&bar[XB_XGEN(bx_)]) == gen, bar);
;             __builtin_amdgcn_fence(__ATOMIC_ACQUIRE, "agent");
;             asm volatile("s_waitcnt vmcnt(0)" ::: "memory");
.LBB0_540:
	s_or_b64 exec, exec, s[6:7]
	s_waitcnt vmcnt(0) lgkmcnt(0)
	s_waitcnt vmcnt(0)

; __device__ __forceinline__ unsigned xb_ld(unsigned* p)              { return __hip_atomic_load(p, __ATOMIC_RELAXED, __HIP_MEMORY_SCOPE_AGENT); }
; __device__ __forceinline__ unsigned xb_add(unsigned* p, unsigned v) { return __hip_atomic_fetch_add(p, v, __ATOMIC_RELAXED, __HIP_MEMORY_SCOPE_AGENT); }
; #define XB_SPIN(cond, bar) do { unsigned _sp = 0; while (cond) { __builtin_amdgcn_s_sleep(1); \
;     if ((++_sp & 255u) == 0u) { if (xb_ld(&(bar)[XB_TMO])) break; if (_sp > XB_SPIN_CAP) { atomicAdd(&(bar)[XB_TMO], 1u); break; } } } } while (0)
; __device__ __forceinline__ void xcd_barrier(const XcdBarrier& b) {
;     ...
;             const unsigned og = xb_add(&bar[XB_TOP], 1u);
;             const unsigned tg = og / nx;
;             if (og + 1u == (tg + 1u) * nx) xb_add(&bar[XB_TOPGEN], 1u);
;             else XB_SPIN(xb_ld(&bar[XB_TOPGEN]) == tg, bar);
;             __builtin_amdgcn_fence(__ATOMIC_ACQUIRE, "agent");
;             xb_add(&bar[XB_XGEN(bx_)], 1u);
;             asm volatile("s_waitcnt vmcnt(0)" ::: "memory");
.LBB0_556:
	s_or_b64 exec, exec, s[4:5]
	s_add_i32 s4, s8, 0x900
	s_mov_b32 s5, 0
	s_lshl_b64 s[4:5], s[4:5], 2
	s_add_u32 s4, s38, s4
	s_addc_u32 s5, s39, s5
	v_mov_b32_e32 v2, 1
	v_mov_b64_e32 v[0:1], s[4:5]
	s_waitcnt vmcnt(0) lgkmcnt(0)
	flat_atomic_add v[0:1], v2
	buffer_inv sc1
	s_waitcnt vmcnt(0)

; __device__ __forceinline__ unsigned xb_ld(unsigned* p)              { return __hip_atomic_load(p, __ATOMIC_RELAXED, __HIP_MEMORY_SCOPE_AGENT); }
; __device__ __forceinline__ unsigned xb_add(unsigned* p, unsigned v) { return __hip_atomic_fetch_add(p, v, __ATOMIC_RELAXED, __HIP_MEMORY_SCOPE_AGENT); }
; #define XB_SPIN(cond, bar) do { unsigned _sp = 0; while (cond) { __builtin_amdgcn_s_sleep(1); \
;     if ((++_sp & 255u) == 0u) { if (xb_ld(&(bar)[XB_TMO])) break; if (_sp > XB_SPIN_CAP) { atomicAdd(&(bar)[XB_TMO], 1u); break; } } } } while (0)
; __device__ __forceinline__ void xcd_barrier(const XcdBarrier& b) {
;     ...
;             const unsigned og = xb_add(&bar[XB_TOP], 1u);
;             const unsigned tg = og / nx;
;             if (og + 1u == (tg + 1u) * nx) xb_add(&bar[XB_TOPGEN], 1u);
;             else XB_SPIN(xb_ld(&bar[XB_TOPGEN]) == tg, bar);
;             __builtin_amdgcn_fence(__ATOMIC_ACQUIRE, "agent");
;             xb_add(&bar[XB_XGEN(bx_)], 1u);
;             asm volatile("s_waitcnt vmcnt(0)" ::: "memory");
.LBB0_702:
	s_or_b64 exec, exec, s[0:1]
	s_add_i32 s64, s2, 0x900
	s_lshl_b64 s[0:1], s[64:65], 2
	s_add_u32 s0, s38, s0
	s_addc_u32 s1, s39, s1
	v_mov_b64_e32 v[0:1], s[0:1]
	s_waitcnt vmcnt(0) lgkmcnt(0)
	flat_atomic_add v[0:1], v249
	buffer_inv sc1
	s_waitcnt vmcnt(0)

; __device__ __forceinline__ unsigned xb_ld(unsigned* p)              { return __hip_atomic_load(p, __ATOMIC_RELAXED, __HIP_MEMORY_SCOPE_AGENT); }
; __device__ __forceinline__ unsigned xb_add(unsigned* p, unsigned v) { return __hip_atomic_fetch_add(p, v, __ATOMIC_RELAXED, __HIP_MEMORY_SCOPE_AGENT); }
; #define XB_SPIN(cond, bar) do { unsigned _sp = 0; while (cond) { __builtin_amdgcn_s_sleep(1); \
;     if ((++_sp & 255u) == 0u) { if (xb_ld(&(bar)[XB_TMO])) break; if (_sp > XB_SPIN_CAP) { atomicAdd(&(bar)[XB_TMO], 1u); break; } } } } while (0)
; __device__ __forceinline__ void xcd_barrier(const XcdBarrier& b) {
;     ...
;         unsigned nloc = b.st[0], nx = b.st[1];
;         if (nloc == 0u) { xcd_barrier_complete(bar, bx_, nloc, nx); b.st[0] = nloc; b.st[1] = nx; }
;         const unsigned old = xb_add(&bar[XB_XSUB(bx_)], 1u);
;         const unsigned gen = old / nloc;
;         if (old + 1u == (gen + 1u) * nloc) {
;             __builtin_amdgcn_fence(__ATOMIC_RELEASE, "agent");
;             asm volatile("s_waitcnt vmcnt(0)" ::: "memory");
;             const unsigned og = xb_add(&bar[XB_TOP], 1u);
;             const unsigned tg = og / nx;
;             if (og + 1u == (tg + 1u) * nx) xb_add(&bar[XB_TOPGEN], 1u);
;             else XB_SPIN(xb_ld(&bar[XB_TOPGEN]) == tg, bar);
;             __builtin_amdgcn_fence(__ATOMIC_ACQUIRE, "agent");
;             xb_add(&bar[XB_XGEN(bx_)], 1u);
;             asm volatile("s_waitcnt vmcnt(0)" ::: "memory");
;         } else {
;             XB_SPIN(xb_ld(&bar[XB_XGEN(bx_)]) == gen, bar);
;             __builtin_amdgcn_fence(__ATOMIC_ACQUIRE, "agent");
;             asm volatile("s_waitcnt vmcnt(0)" ::: "memory");
;         }
.LBB0_771:
	s_lshl_b32 s2, s2, 6
	s_add_i32 s64, s2, 0x500
	s_lshl_b64 s[0:1], s[64:65], 2
	s_add_u32 s0, s38, s0
	s_addc_u32 s1, s39, s1
	v_mov_b64_e32 v[4:5], s[0:1]
	flat_atomic_add v3, v[4:5], v249 sc0
	v_cvt_f32_u32_e32 v1, v2
	v_sub_u32_e32 v4, 0, v2
	v_rcp_iflag_f32_e32 v1, v1
	s_nop 0
	v_mul_f32_e32 v1, 0x4f7ffffe, v1
	v_cvt_u32_f32_e32 v1, v1
	v_mul_lo_u32 v4, v4, v1
	v_mul_hi_u32 v4, v1, v4
	v_add_u32_e32 v1, v1, v4
	s_waitcnt vmcnt(0) lgkmcnt(0)
	v_mul_hi_u32 v1, v3, v1
	v_mul_lo_u32 v4, v1, v2
	v_sub_u32_e32 v4, v3, v4
	v_cmp_ge_u32_e32 vcc, v4, v2
	v_add_u32_e32 v5, 1, v1
	s_nop 0
	v_cndmask_b32_e32 v1, v1, v5, vcc
	v_sub_u32_e32 v5, v4, v2
	v_cndmask_b32_e32 v4, v4, v5, vcc
	v_cmp_ge_u32_e32 vcc, v4, v2
	v_add_u32_e32 v4, 1, v1
	s_nop 0
	v_cndmask_b32_e32 v1, v1, v4, vcc
	v_add_u32_e32 v4, 1, v3
	v_mad_u64_u32 v[2:3], s[0:1], v2, v1, v[2:3]
	v_cmp_ne_u32_e32 vcc, v4, v2
	s_and_saveexec_b64 s[0:1], vcc
	s_xor_b64 s[0:1], exec, s[0:1]
	s_cbranch_execz .LBB0_784
	s_add_i32 s64, s2, 0x900
	s_lshl_b64 s[4:5], s[64:65], 2
	s_add_u32 s6, s38, s4
	s_addc_u32 s7, s39, s5
	v_mov_b64_e32 v[2:3], s[6:7]
	buffer_inv sc1
	flat_load_dword v0, v[2:3] sc1
	s_waitcnt vmcnt(0) lgkmcnt(0)
	v_cmp_eq_u32_e32 vcc, v0, v1
	s_and_saveexec_b64 s[4:5], vcc
	s_cbranch_execz .LBB0_783
	s_mov_b32 s3, 1
	s_mov_b64 s[10:11], 0
	s_branch .LBB0_775

; __device__ __forceinline__ unsigned xb_ld(unsigned* p)              { return __hip_atomic_load(p, __ATOMIC_RELAXED, __HIP_MEMORY_SCOPE_AGENT); }
; #define XB_SPIN(cond, bar) do { unsigned _sp = 0; while (cond) { __builtin_amdgcn_s_sleep(1); \
;     if ((++_sp & 255u) == 0u) { if (xb_ld(&(bar)[XB_TMO])) break; if (_sp > XB_SPIN_CAP) { atomicAdd(&(bar)[XB_TMO], 1u); break; } } } } while (0)
; __device__ __forceinline__ void xcd_barrier(const XcdBarrier& b) {
;     ...
;             XB_SPIN(xb_ld(&bar[XB_XGEN(bx_)]) == gen, bar);
;             __builtin_amdgcn_fence(__ATOMIC_ACQUIRE, "agent");
;             asm volatile("s_waitcnt vmcnt(0)" ::: "memory");
.LBB0_783:
	s_or_b64 exec, exec, s[4:5]
	s_waitcnt vmcnt(0) lgkmcnt(0)
	s_waitcnt vmcnt(0)
